# v28 = v27 + GLA-scan conversion tiles paired like the others (both 64-byte halves of an output line from adjacent waves of one workgroup)
# speedup vs baseline: 1.0129x; 1.0089x over previous
; #define CT_LOADNT(T_) do { const int tt_ = (T_) < CT_TOTAL ? (T_) : CT_TOTAL - 1; const ConvTile ct_ = conv_tile_desc(cttab, tt_); const int ckq_ = lane >> 4, ccol_ = ((lane & 15) * 4 < ct_.nvalid) ? (lane & 15) * 4 : 0; CT_FORQ(CT_LOAD1NT) } while (0)
; __device__ __forceinline__ ConvTile conv_tile_desc(const unsigned long long* tab, int t) {
;     int si, di, N, K, nb, kb, e = 0, mode = 0, npad = 0;
;     if (t < CT_L0A) { si = 0; di = 10; N = L0C; K = DM; nb = t % 104; kb = t / 104; npad = 1; }
;     else if (t < CT_L0B) { const int u = t - CT_L0A; si = 1; di = 11; N = DM; K = DM; nb = u & 31; kb = u >> 5; }
;     else if (t < CT_L0C) { const int u = t - CT_L0B; si = 2; di = 12; N = FFN; K = DM; nb = u % 176; kb = u / 176; mode = 1; }
;     else if (t < CT_L0) { const int u = t - CT_L0C; si = 4; di = 13; N = DM; K = FFN; nb = u & 31; kb = u >> 5; }
;     else if (t < CT_A) { const int u = t - CT_L0; si = 5; di = 14; N = L1C; K = DM; nb = u % 100; kb = u / 100; npad = 1; }
;     else if (t < CT_B) { const int u = t - CT_A; si = 6; di = 15; N = DM; K = DM; nb = u & 31; kb = u >> 5; }
;     else if (t < CT_C) { const int u = t - CT_B; e = u / 14336; const int v = u % 14336; si = 7; di = 16; N = EXD; K = DM; nb = v % 224; kb = v / 224; mode = 1; }
;     else { const int u = (t < CT_TOTAL ? t : CT_TOTAL - 1) - CT_C; e = u / 7168; const int v = u % 7168; si = 9; di = 17; N = DM; K = EXD; nb = v & 31; kb = v >> 5; }
;     const int n0 = nb * 64;
;     int col0 = n0, nvalid = 64;
;     if (mode) { col0 = (n0 >> 8) * 128 + (n0 & 127); si += (n0 >> 7) & 1; }
;     if (npad) { nvalid = N - n0; if (nvalid <= 0) col0 = 0; }
; __device__ __forceinline__ void ph_glascan(const Params& p, float* lds, int wg, int nwg, int gct_begin) {
;     ...
;         pg8::bf16x8 cqt[8], cam[2], ckh[2][2], cvt[2][2], nkh[2][2], nvt[2][2]; pg8::f32x4 cdec[2], ndec[2];
;         const pg8::bf16x8 zz = {0, 0, 0, 0, 0, 0, 0, 0};
; #pragma unroll
;         for (int ks = 0; ks < 8; ++ks) cqt[ks] = zz;
; #pragma unroll
;         for (int ks = 0; ks < 2; ++ks) cam[ks] = zz;
;         GLA_LOAD_S(ckh, cvt, cdec, 0);
;         float4 cv0, cv1, cv2, cv3, cv4, cv5, cv6, cv7; CT_LOADNT(gct_begin + wg * 8 + w);
;         const int gct_nch = (CT_TOTAL - gct_begin + nwg * 8 - 1) / (nwg * 8);
.LBB0_1594:
	s_or_b64 exec, exec, s[0:1]
	v_readlane_b32 s0, v248, 43
	v_mov_b32_e32 v4, v0
	v_readlane_b32 s1, v248, 44
	s_waitcnt lgkmcnt(0)
	s_barrier
	s_and_b64 vcc, exec, s[0:1]
	v_readfirstlane_b32 s6, v4
	s_cbranch_vccz .LBB0_1704
	v_writelane_b32 v248, s85, 49
	s_mul_i32 s2, s96, 0x220
	v_readlane_b32 s0, v248, 38
	s_add_i32 s0, s0, s2
	v_readlane_b32 s12, v248, 25
	s_add_i32 s3, s0, s12
	s_ashr_i32 s5, s6, 6
	s_sub_i32 s1, s88, s0
	s_add_i32 s29, s3, s5
	s_add_i32 s1, s1, 0x324ff
	s_ashr_i32 s4, s6, 7
	s_lshl_b32 s0, s5, 5
	s_min_i32 s7, s29, 0x324ff
	s_cmpk_gt_i32 s29, 0x19ff
	s_cselect_b64 s[72:73], -1, 0
	s_cmpk_gt_i32 s29, 0x21ff
	s_cselect_b64 s[74:75], -1, 0
	s_cmpk_gt_i32 s29, 0x4dff
	s_cselect_b64 s[80:81], -1, 0
	s_cmpk_gt_i32 s29, 0x63ff
	s_cselect_b64 s[8:9], -1, 0
	v_writelane_b32 v247, s8, 35
	s_cmpk_gt_i32 s29, 0x7cff
	v_readlane_b32 s13, v248, 26
	v_writelane_b32 v247, s9, 36
	s_cselect_b64 s[8:9], -1, 0
	v_writelane_b32 v248, s8, 53
	s_cmp_gt_i32 s29, 0x84ff
	s_mul_i32 s28, s96, 0x218
	v_writelane_b32 v248, s9, 54
	s_cselect_b64 s[8:9], -1, 0
	s_add_i32 s3, s7, 0xbb00
	s_bfe_u32 s20, s3, 0x6000a
	s_mulk_i32 s20, 0x2493
	s_lshr_b32 s26, s20, 16
	s_mul_i32 s20, s26, 0x1c00
	s_sub_i32 s3, s3, s20
	s_and_b32 s32, s3, 1
	s_bfe_u32 s30, s3, 0x50001
	s_bfe_u32 s31, s3, 0xa0006
	s_lshl_b32 s31, s31, 1
	s_or_b32 s31, s31, s32
	s_add_i32 s3, s7, 0xffff7b00
	s_lshr_b32 s20, s3, 11
	s_mul_hi_u32 s34, s20, 0x24924925
	s_mul_i32 s20, s34, 0x3800
	s_sub_i32 s3, s3, s20
	s_bfe_u32 s20, s3, 0x100005
	s_mulk_i32 s20, 0x2493
	s_lshr_b32 s35, s20, 16
	s_mul_i32 s20, s35, 0xe0
	v_writelane_b32 v248, s8, 51
	s_sub_i32 s3, s3, s20
	s_add_i32 s20, s7, 0xffff8300
	v_writelane_b32 v248, s9, 52
	s_lshr_b32 s8, s20, 5
	s_add_i32 s20, s7, 0x9c00
	s_bfe_u32 s21, s20, 0xe0002
	s_mulk_i32 s21, 0x147b
	s_lshr_b32 s27, s21, 17
	s_mul_i32 s21, s27, 0x64
	s_sub_i32 s20, s20, s21
	s_and_b32 s33, s20, 0xffff
	s_add_i32 s20, s7, 0xffffb200
	s_lshr_b32 s45, s20, 5
	s_add_i32 s20, s7, 0xde00
	s_and_b32 s21, s20, 0xffff
	s_mul_i32 s21, s21, 0xba2f
	s_lshr_b32 s47, s21, 23
	s_mul_i32 s21, s47, 0xb0
	s_sub_i32 s20, s20, s21
	s_abs_i32 s21, s88
	v_cvt_f32_u32_e32 v2, s21
	s_and_b32 s65, s20, 0xffff
	s_add_i32 s20, s7, 0xffffe600
	s_lshr_b32 s66, s20, 5
	v_rcp_iflag_f32_e32 v2, v2
	s_mul_hi_i32 s20, s7, 0x4ec4ec4f
	s_lshr_b32 s22, s20, 31
	s_ashr_i32 s67, s20, 5
	v_mul_f32_e32 v2, 0x4f7ffffe, v2
	v_cvt_u32_f32_e32 v2, v2
	s_add_i32 s67, s67, s22
	s_mul_i32 s20, s67, 0x68
	s_sub_i32 s68, s7, s20
	s_sub_i32 s20, 0, s21
	v_readfirstlane_b32 s22, v2
	s_mul_i32 s20, s20, s22
	s_mul_hi_u32 s20, s22, s20
	s_and_b32 s36, s3, 0xffff
	s_and_b32 s3, s7, 31
	s_xor_b32 s7, s1, s88
	s_abs_i32 s1, s1
	s_add_i32 s22, s22, s20
	s_mul_hi_u32 s20, s1, s22
	s_mul_i32 s22, s20, s21
	s_sub_i32 s1, s1, s22
	s_ashr_i32 s7, s7, 31
	s_add_i32 s22, s20, 1
	s_sub_i32 s23, s1, s21
	s_cmp_ge_u32 s1, s21
	s_cselect_b32 s20, s22, s20
	s_cselect_b32 s1, s23, s1
	s_add_i32 s22, s20, 1
	s_cmp_ge_u32 s1, s21
	s_cselect_b32 s1, s22, s20
	s_xor_b32 s1, s1, s7
	s_mov_b32 s69, 5
	s_lshl_b32 s1, s5, 4
	s_and_b32 s70, s6, 0xffffffc0
	s_and_b32 s7, s1, 16
	s_bitcmp1_b32 s5, 0
	s_cselect_b64 s[82:83], -1, 0
	s_ashr_i32 s1, s0, 31
	s_cmp_gt_i32 s29, 0x244ff
	v_writelane_b32 v248, s8, 5
	s_cselect_b64 s[8:9], -1, 0
	v_writelane_b32 v248, s8, 59
	s_and_b64 s[24:25], s[8:9], exec
	s_movk_i32 s25, 0x800
	v_writelane_b32 v248, s9, 60
	s_cselect_b32 s8, s26, s34
	v_writelane_b32 v245, s8, 13
	s_mov_b32 s86, s88
	v_mov_b32_e32 v3, 0
	v_writelane_b32 v245, s9, 14
	s_cselect_b32 s8, s31, s35
	v_writelane_b32 v248, s8, 38
	s_cselect_b32 s8, s30, s36
	v_writelane_b32 v248, s8, 61
	s_cselect_b32 s8, 0x1c00, s25
	v_writelane_b32 v245, s8, 10
	v_and_b32_e32 v2, 48, v4
	v_and_b32_e32 v5, 63, v4
	v_writelane_b32 v245, s9, 11
	s_cselect_b32 s8, s25, 0x1c00
	v_writelane_b32 v245, s8, 12
	s_cselect_b32 s8, 9, 7
	s_add_i32 s44, s70, 0
	s_add_i32 s46, s29, s28
	s_cmpk_gt_i32 s69, 0x43
	s_cselect_b64 s[28:29], -1, 0
	s_min_i32 s50, s46, 0x324ff
	s_cmpk_gt_i32 s46, 0x19ff
	s_cselect_b64 s[30:31], -1, 0
	s_cmpk_gt_u32 s46, 0x21ff
	s_cselect_b64 s[34:35], -1, 0
	s_cmpk_gt_u32 s46, 0x4dff
	v_writelane_b32 v248, s8, 57
	s_cselect_b64 s[8:9], -1, 0
	v_writelane_b32 v248, s8, 45
	s_cmpk_gt_u32 s46, 0x63ff
	v_lshlrev_b32_e32 v159, 3, v5
	v_writelane_b32 v248, s9, 46
	s_cselect_b64 s[8:9], -1, 0
	v_writelane_b32 v248, s8, 47
	s_cmpk_gt_u32 s46, 0x7cff
	v_lshl_or_b32 v8, s5, 11, v159
	v_writelane_b32 v248, s9, 48
	s_cselect_b64 s[8:9], -1, 0
	v_writelane_b32 v245, s8, 3
	s_cmpk_gt_u32 s46, 0x84ff
	v_bfe_u32 v5, v4, 4, 2
	v_writelane_b32 v245, s9, 4
; #define CT_LOADNT(T_) do { const int tt_ = (T_) < CT_TOTAL ? (T_) : CT_TOTAL - 1; const ConvTile ct_ = conv_tile_desc(cttab, tt_); const int ckq_ = lane >> 4, ccol_ = ((lane & 15) * 4 < ct_.nvalid) ? (lane & 15) * 4 : 0; CT_FORQ(CT_LOAD1NT) } while (0)
; __device__ __forceinline__ ConvTile conv_tile_desc(const unsigned long long* tab, int t) {
;     int si, di, N, K, nb, kb, e = 0, mode = 0, npad = 0;
;     if (t < CT_L0A) { si = 0; di = 10; N = L0C; K = DM; nb = t % 104; kb = t / 104; npad = 1; }
;     else if (t < CT_L0B) { const int u = t - CT_L0A; si = 1; di = 11; N = DM; K = DM; nb = u & 31; kb = u >> 5; }
;     else if (t < CT_L0C) { const int u = t - CT_L0B; si = 2; di = 12; N = FFN; K = DM; nb = u % 176; kb = u / 176; mode = 1; }
;     else if (t < CT_L0) { const int u = t - CT_L0C; si = 4; di = 13; N = DM; K = FFN; nb = u & 31; kb = u >> 5; }
;     else if (t < CT_A) { const int u = t - CT_L0; si = 5; di = 14; N = L1C; K = DM; nb = u % 100; kb = u / 100; npad = 1; }
;     else if (t < CT_B) { const int u = t - CT_A; si = 6; di = 15; N = DM; K = DM; nb = u & 31; kb = u >> 5; }
;     else if (t < CT_C) { const int u = t - CT_B; e = u / 14336; const int v = u % 14336; si = 7; di = 16; N = EXD; K = DM; nb = v % 224; kb = v / 224; mode = 1; }
;     else { const int u = (t < CT_TOTAL ? t : CT_TOTAL - 1) - CT_C; e = u / 7168; const int v = u % 7168; si = 9; di = 17; N = DM; K = EXD; nb = v & 31; kb = v >> 5; }
;     const int n0 = nb * 64;
;     int col0 = n0, nvalid = 64;
;     if (mode) { col0 = (n0 >> 8) * 128 + (n0 & 127); si += (n0 >> 7) & 1; }
;     if (npad) { nvalid = N - n0; if (nvalid <= 0) col0 = 0; }
; __device__ __forceinline__ void ph_glascan(const Params& p, float* lds, int wg, int nwg, int gct_begin) {
;     ...
;         GLA_LOAD_S(ckh, cvt, cdec, 0);
;         float4 cv0, cv1, cv2, cv3, cv4, cv5, cv6, cv7; CT_LOADNT(gct_begin + wg * 8 + w);
;         const int gct_nch = (CT_TOTAL - gct_begin + nwg * 8 - 1) / (nwg * 8);
	s_cselect_b64 s[8:9], -1, 0
	s_cmp_lt_u32 s46, 0x24500
	s_cselect_b64 s[48:49], -1, 0
	s_add_i32 s46, s50, 0xbb00
	s_bfe_u32 s51, s46, 0x6000a
	s_mulk_i32 s51, 0x2493
	s_lshr_b32 s51, s51, 16
	s_mul_i32 s52, s51, 0x1c00
	s_sub_i32 s46, s46, s52
	s_add_i32 s52, s50, 0xffff7b00
	s_lshr_b32 s53, s52, 11
	s_mul_hi_u32 s53, s53, 0x24924925
	s_mul_i32 s54, s53, 0x3800
	s_sub_i32 s52, s52, s54
	s_bfe_u32 s54, s52, 0x100005
	s_mulk_i32 s54, 0x2493
	s_lshr_b32 s54, s54, 16
	s_mul_i32 s55, s54, 0xe0
	s_sub_i32 s52, s52, s55
	s_add_i32 s55, s50, 0x9c00
	s_bfe_u32 s56, s55, 0xe0002
	s_mulk_i32 s56, 0x147b
	s_lshr_b32 s79, s56, 17
	s_mul_i32 s56, s79, 0x64
	s_sub_i32 s55, s55, s56
	s_add_i32 s56, s50, 0xde00
	s_and_b32 s57, s56, 0xffff
	s_mul_i32 s57, s57, 0xba2f
	s_lshr_b32 s76, s57, 23
	s_mul_i32 s57, s76, 0xb0
	s_sub_i32 s56, s56, s57
	s_mul_hi_i32 s57, s50, 0x4ec4ec4f
	s_lshr_b32 s58, s57, 31
	s_ashr_i32 s77, s57, 5
	v_writelane_b32 v248, s8, 55
	s_add_i32 s77, s77, s58
	s_add_i32 s58, s50, 0xffff8300
	v_writelane_b32 v248, s9, 56
	s_lshr_b32 s8, s58, 5
	v_writelane_b32 v245, s8, 9
	s_and_b32 s8, s55, 0xffff
	s_add_i32 s55, s50, 0xffffb200
	s_lshr_b32 s26, s55, 5
	s_mul_i32 s55, s77, 0x68
	s_sub_i32 s87, s50, s55
	s_and_b32 s24, s50, 31
	s_addk_i32 s50, 0xe600
	s_and_b32 s32, s46, 1
	s_bfe_u32 s57, s46, 0x50001
	s_bfe_u32 s46, s46, 0xa0006
	s_lshl_b32 s46, s46, 1
	s_or_b32 s46, s46, s32
	s_and_b32 s52, s52, 0xffff
	s_and_b32 s71, s56, 0xffff
	s_lshr_b32 s88, s50, 5
	v_cndmask_b32_e64 v158, 0, 1, s[48:49]
	s_and_b64 s[48:49], s[48:49], exec
	v_writelane_b32 v248, s8, 63
	s_cselect_b32 s8, s52, s57
	v_writelane_b32 v245, s8, 1
	s_cselect_b32 s8, s54, s46
	v_writelane_b32 v245, s8, 6
	s_cselect_b32 s8, s53, s51
	v_writelane_b32 v245, s8, 7
	v_readlane_b32 s36, v248, 29
	v_readlane_b32 s38, v248, 31
	v_writelane_b32 v245, s9, 8
	s_cselect_b32 s8, 16, 17
	v_writelane_b32 v245, s8, 15
	s_cselect_b32 s8, 0x1c00, s25
	v_writelane_b32 v245, s8, 5
	s_cselect_b32 s8, s25, 0x1c00
	v_writelane_b32 v245, s8, 17
	v_readlane_b32 s39, v248, 32
	s_lshl_b32 s6, s6, 3
	v_writelane_b32 v245, s9, 18
	v_readlane_b32 s8, v248, 37
	s_add_i32 s25, s5, s8
	s_add_i32 s89, s25, s12
	v_lshl_add_u64 v[6:7], s[38:39], 0, v[2:3]
	s_lshl_b64 s[0:1], s[0:1], 2
	s_addk_i32 s89, 0x6400
	s_and_b32 s6, s6, 0xfffffc00
	s_lshl_b32 s94, s90, 1
	s_lshl_b32 s95, s96, 1
	v_lshl_add_u64 v[160:161], v[6:7], 0, s[0:1]
	s_add_u32 s0, s38, s0
	v_or_b32_e32 v10, s6, v159
	v_and_b32_e32 v11, 15, v4
	v_readlane_b32 s48, v248, 9
	s_addc_u32 s1, s39, s1
	v_lshlrev_b32_e32 v162, 3, v5
	v_lshl_or_b32 v13, s4, 4, v11
	v_lshl_or_b32 v12, s4, 12, v159
	v_lshlrev_b32_e32 v14, 2, v5
	v_lshlrev_b32_e32 v164, 2, v11
	v_or_b32_e32 v5, s7, v11
	v_ashrrev_i32_e32 v9, 31, v8
	v_mul_u32_u24_e32 v197, 0x210, v11
	v_readlane_b32 s49, v248, 10
	v_readlane_b32 s50, v248, 11
	v_readlane_b32 s51, v248, 12
	v_readlane_b32 s60, v248, 21
	v_readlane_b32 s61, v248, 22
	v_readlane_b32 s62, v248, 23
	v_readlane_b32 s63, v248, 24
	v_ashrrev_i32_e32 v11, 31, v10
	v_readlane_b32 s37, v248, 30
	s_mov_b64 s[84:85], s[96:97]
	v_lshl_add_u64 v[6:7], s[0:1], 0, v[2:3]
	v_add_u32_e32 v15, s44, v162
	v_mul_u32_u24_e32 v196, 0x210, v5
	v_add_u32_e32 v199, 0xfc0, v13
	v_sub_u32_e32 v200, 63, v13
	v_readlane_b32 s53, v248, 14
	v_readlane_b32 s58, v248, 19
	v_readlane_b32 s59, v248, 20
	v_lshl_add_u64 v[166:167], v[8:9], 1, s[60:61]
	v_add_u32_e32 v203, 0xffffff00, v13
	v_sub_u32_e32 v204, 0x10ff, v13
	v_lshl_add_u64 v[8:9], v[10:11], 1, s[62:63]
	s_mov_b64 s[48:49], 0x2000
	s_mov_b64 s[50:51], 0x400
	v_ashrrev_i32_e32 v13, 31, v12
	s_add_u32 s96, s36, 0x10000
	s_movk_i32 s0, 0x1080
	v_or_b32_e32 v189, 1, v162
	v_or_b32_e32 v190, 2, v162
	v_or_b32_e32 v191, 3, v162
	v_or_b32_e32 v192, 4, v162
	v_or_b32_e32 v193, 5, v162
	v_or_b32_e32 v194, 6, v162
	v_or_b32_e32 v195, 7, v162
	v_add3_u32 v198, 0, v196, v2
	v_add_u32_e32 v201, 0xfffffe00, v4
	v_lshl_add_u32 v202, v4, 2, 0
	v_lshl_add_u64 v[168:169], v[8:9], 0, s[48:49]
	v_lshl_add_u64 v[170:171], v[6:7], 0, s[50:51]
	v_lshl_add_u64 v[172:173], v[12:13], 1, s[58:59]
	s_addc_u32 s97, s37, 0
	s_lshl_b32 s4, s7, 2
	v_lshlrev_b32_e32 v174, 2, v14
	v_add_u32_e32 v205, v15, v197
	v_cmp_gt_i32_e64 s[0:1], s0, v4
	s_add_i32 s5, 0, 0x4200
	s_mov_b64 s[38:39], s[90:91]
	s_mov_b32 s64, s90
	s_mov_b32 s53, 0
	v_readlane_b32 s40, v248, 33
	v_readlane_b32 s41, v248, 34
	v_readlane_b32 s42, v248, 35
	v_readlane_b32 s43, v248, 36
	v_readlane_b32 s52, v248, 13
	v_readlane_b32 s54, v248, 15
	v_readlane_b32 s55, v248, 16
	v_readlane_b32 s56, v248, 17
	v_readlane_b32 s57, v248, 18
	s_branch .LBB0_1599

; __device__ __forceinline__ ConvTile conv_tile_desc(const unsigned long long* tab, int t) {
;     int si, di, N, K, nb, kb, e = 0, mode = 0, npad = 0;
;     if (t < CT_L0A) { si = 0; di = 10; N = L0C; K = DM; nb = t % 104; kb = t / 104; npad = 1; }
;     else if (t < CT_L0B) { const int u = t - CT_L0A; si = 1; di = 11; N = DM; K = DM; nb = u & 31; kb = u >> 5; }
;     else if (t < CT_L0C) { const int u = t - CT_L0B; si = 2; di = 12; N = FFN; K = DM; nb = u % 176; kb = u / 176; mode = 1; }
;     else if (t < CT_L0) { const int u = t - CT_L0C; si = 4; di = 13; N = DM; K = FFN; nb = u & 31; kb = u >> 5; }
;     else if (t < CT_A) { const int u = t - CT_L0; si = 5; di = 14; N = L1C; K = DM; nb = u % 100; kb = u / 100; npad = 1; }
;     else if (t < CT_B) { const int u = t - CT_A; si = 6; di = 15; N = DM; K = DM; nb = u & 31; kb = u >> 5; }
;     else if (t < CT_C) { const int u = t - CT_B; e = u / 14336; const int v = u % 14336; si = 7; di = 16; N = EXD; K = DM; nb = v % 224; kb = v / 224; mode = 1; }
;     else { const int u = (t < CT_TOTAL ? t : CT_TOTAL - 1) - CT_C; e = u / 7168; const int v = u % 7168; si = 9; di = 17; N = DM; K = EXD; nb = v & 31; kb = v >> 5; }
;     const int n0 = nb * 64;
;     int col0 = n0, nvalid = 64;
;     if (mode) { col0 = (n0 >> 8) * 128 + (n0 & 127); si += (n0 >> 7) & 1; }
;     if (npad) { nvalid = N - n0; if (nvalid <= 0) col0 = 0; }
.LBB0_1625:
	s_add_i32 vcc_lo, s2, s93
	s_min_i32 s52, vcc_lo, 0x324ff
	s_cmpk_gt_i32 vcc_lo, 0x19ff
	s_mov_b64 s[62:63], -1
	s_cbranch_scc0 .LBB0_1650
	s_cmpk_gt_u32 vcc_lo, 0x21ff
	s_cbranch_scc0 .LBB0_1647
	s_cmpk_gt_u32 vcc_lo, 0x4dff
	s_cbranch_scc0 .LBB0_1644
	s_cmpk_gt_u32 vcc_lo, 0x63ff
	s_cbranch_scc0 .LBB0_1641
	s_mov_b64 s[58:59], -1
	s_cmpk_gt_u32 vcc_lo, 0x7cff
	s_cbranch_scc0 .LBB0_1638
	s_cmpk_gt_u32 vcc_lo, 0x84ff
	s_cbranch_scc0 .LBB0_1635
	s_cmp_gt_u32 vcc_lo, 0x244ff
	s_mov_b64 s[56:57], -1
	s_cbranch_scc0 .LBB0_1633
	s_add_i32 s25, s52, 0xbb00
	s_bfe_u32 s46, s25, 0x6000a
	s_mulk_i32 s46, 0x2493
	s_lshr_b32 s46, s46, 16
	s_mul_i32 s56, s46, 0x1c00
	s_sub_i32 s25, s25, s56
	s_and_b32 s32, s25, 1
	s_bfe_u32 s91, s25, 0x50001
	s_bfe_u32 s90, s25, 0xa0006
	s_lshl_b32 s90, s90, 1
	s_or_b32 s90, s90, s32
	s_mov_b64 s[56:57], 0

; __device__ __forceinline__ ConvTile conv_tile_desc(const unsigned long long* tab, int t) {
;     int si, di, N, K, nb, kb, e = 0, mode = 0, npad = 0;
;     if (t < CT_L0A) { si = 0; di = 10; N = L0C; K = DM; nb = t % 104; kb = t / 104; npad = 1; }
;     else if (t < CT_L0B) { const int u = t - CT_L0A; si = 1; di = 11; N = DM; K = DM; nb = u & 31; kb = u >> 5; }
;     else if (t < CT_L0C) { const int u = t - CT_L0B; si = 2; di = 12; N = FFN; K = DM; nb = u % 176; kb = u / 176; mode = 1; }
;     else if (t < CT_L0) { const int u = t - CT_L0C; si = 4; di = 13; N = DM; K = FFN; nb = u & 31; kb = u >> 5; }
;     else if (t < CT_A) { const int u = t - CT_L0; si = 5; di = 14; N = L1C; K = DM; nb = u % 100; kb = u / 100; npad = 1; }
;     else if (t < CT_B) { const int u = t - CT_A; si = 6; di = 15; N = DM; K = DM; nb = u & 31; kb = u >> 5; }
;     else if (t < CT_C) { const int u = t - CT_B; e = u / 14336; const int v = u % 14336; si = 7; di = 16; N = EXD; K = DM; nb = v % 224; kb = v / 224; mode = 1; }
;     else { const int u = (t < CT_TOTAL ? t : CT_TOTAL - 1) - CT_C; e = u / 7168; const int v = u % 7168; si = 9; di = 17; N = DM; K = EXD; nb = v & 31; kb = v >> 5; }
;     const int n0 = nb * 64;
;     int col0 = n0, nvalid = 64;
;     if (mode) { col0 = (n0 >> 8) * 128 + (n0 & 127); si += (n0 >> 7) & 1; }
;     if (npad) { nvalid = N - n0; if (nvalid <= 0) col0 = 0; }
.Lgla_wd:
	v_cvt_pk_bf16_f32 v2, v74, v78
	v_cvt_pk_bf16_f32 v134, v86, v94
	v_cvt_pk_bf16_f32 v135, v102, v114
	v_cvt_pk_bf16_f32 v136, v126, v130
	v_cmp_gt_i32_e32 vcc, s63, v164
	s_lshl_b64 s[56:57], s[56:57], 1
	s_cmp_ge_i32 s44, s69
	v_cndmask_b32_e32 v137, 0, v136, vcc
	v_cndmask_b32_e32 v136, 0, v135, vcc
	v_cndmask_b32_e32 v135, 0, v134, vcc
	v_cndmask_b32_e32 v134, 0, v2, vcc
	global_store_dwordx4 v[4:5], v[134:137], off
	v_cvt_pk_bf16_f32 v2, v75, v79
	v_lshl_add_u64 v[4:5], v[4:5], 0, s[56:57]
	v_cvt_pk_bf16_f32 v134, v87, v95
	v_cvt_pk_bf16_f32 v135, v103, v115
	v_cvt_pk_bf16_f32 v136, v127, v131
	v_cndmask_b32_e32 v137, 0, v136, vcc
	v_cndmask_b32_e32 v136, 0, v135, vcc
	v_cndmask_b32_e32 v135, 0, v134, vcc
	v_cndmask_b32_e32 v134, 0, v2, vcc
	global_store_dwordx4 v[4:5], v[134:137], off
	v_cvt_pk_bf16_f32 v2, v76, v80
	v_lshl_add_u64 v[4:5], v[4:5], 0, s[56:57]
	v_cvt_pk_bf16_f32 v134, v88, v96
	v_cvt_pk_bf16_f32 v135, v104, v116
	v_cvt_pk_bf16_f32 v136, v128, v132
	v_cndmask_b32_e32 v137, 0, v136, vcc
	v_cndmask_b32_e32 v136, 0, v135, vcc
	v_cndmask_b32_e32 v135, 0, v134, vcc
	v_cndmask_b32_e32 v134, 0, v2, vcc
	global_store_dwordx4 v[4:5], v[134:137], off
	v_cvt_pk_bf16_f32 v2, v77, v81
	v_lshl_add_u64 v[4:5], v[4:5], 0, s[56:57]
	v_cvt_pk_bf16_f32 v134, v89, v97
	v_cvt_pk_bf16_f32 v135, v105, v117
	v_cvt_pk_bf16_f32 v136, v129, v133
	v_cndmask_b32_e32 v137, 0, v136, vcc
	v_cndmask_b32_e32 v136, 0, v135, vcc
	v_cndmask_b32_e32 v135, 0, v134, vcc
	v_cndmask_b32_e32 v134, 0, v2, vcc
	global_store_dwordx4 v[4:5], v[134:137], off
	s_cbranch_scc1 .LBB0_1681
	s_mul_i32 vcc_lo, s84, 0x228
	s_add_i32 vcc_lo, vcc_lo, s93
	s_min_i32 s90, vcc_lo, 0x324ff
	s_cmpk_gt_i32 vcc_lo, 0x19ff
	s_mov_b64 s[62:63], -1
	s_cbranch_scc0 .LBB0_1678
	s_cmpk_gt_u32 vcc_lo, 0x21ff
	s_cbranch_scc0 .LBB0_1675
	s_cmpk_gt_u32 vcc_lo, 0x4dff
	s_cbranch_scc0 .LBB0_1672
	s_cmpk_gt_u32 vcc_lo, 0x63ff
	s_cbranch_scc0 .LBB0_1669
	s_mov_b64 s[56:57], -1
	s_cmpk_gt_u32 vcc_lo, 0x7cff
	s_cbranch_scc0 .LBB0_1666
	s_cmpk_gt_u32 vcc_lo, 0x84ff
	s_cbranch_scc0 .LBB0_1663
	s_mov_b64 s[58:59], -1
	s_cmp_gt_u32 vcc_lo, 0x244ff
	s_mov_b64 s[60:61], -1
	s_cbranch_scc0 .LBB0_1661
	s_add_i32 s25, s90, 0xbb00
	s_bfe_u32 s46, s25, 0x6000a
	s_mulk_i32 s46, 0x2493
	s_lshr_b32 s46, s46, 16
	s_mul_i32 s52, s46, 0x1c00
	s_sub_i32 s25, s25, s52
	s_and_b32 s32, s25, 1
	s_bfe_u32 s92, s25, 0x50001
	s_bfe_u32 s91, s25, 0xa0006
	s_lshl_b32 s91, s91, 1
	s_or_b32 s91, s91, s32
	s_mov_b64 s[60:61], 0
